# norm1 after an MoE layer: the two expert-output rows (ycomb) are loaded one row iteration ahead into spare registers instead of being loaded and waited inside each iteration
# speedup vs baseline: 1.0074x; 1.0032x over previous
.LBB0_58:
	v_readlane_b32 s10, v255, 15
	s_cmp_lg_u32 s10, 0
	v_readlane_b32 s8, v255, 19
	s_cselect_b64 s[4:5], -1, 0
	v_readlane_b32 s9, v255, 20
	s_and_b64 s[4:5], s[4:5], s[8:9]
	s_add_u32 s8, s16, 0x5c00000
	s_addc_u32 s9, s17, 0
	s_and_b64 s[4:5], s[4:5], exec
	s_cselect_b32 s5, s9, 0
	s_cselect_b32 s4, s8, 0
	s_cmp_lg_u64 s[4:5], 0
	s_cselect_b64 s[22:23], -1, 0
	s_lshl_b32 s52, s10, 3
	s_lshl_b64 s[8:9], s[52:53], 2
	s_waitcnt lgkmcnt(0)
	s_add_u32 s24, s6, s8
	v_and_b32_e32 v20, 4, v22
	v_readlane_b32 s11, v255, 16
	s_addc_u32 s25, s7, s9
	v_cmp_eq_u32_e64 s[8:9], 0, v20
	v_and_b32_e32 v20, 2, v22
	v_cmp_eq_u32_e64 s[10:11], 0, v20
	v_and_b32_e32 v20, 1, v22
	v_cmp_ne_u32_e64 s[6:7], 0, v19
	v_cmp_eq_u32_e64 s[12:13], 0, v20
	v_cmp_gt_u32_e64 s[14:15], 8, v19
	v_lshlrev_b32_e32 v20, 2, v19
	v_and_b32_e32 v19, 64, v234
	v_add_u32_e32 v19, 64, v19
	v_xor_b32_e32 v22, 1, v234
	v_cmp_lt_i32_e32 vcc, v22, v19
	v_mov_b32_e32 v21, v1
	v_lshl_add_u64 v[206:207], s[24:25], 0, v[20:21]
	v_cndmask_b32_e32 v22, v234, v22, vcc
	v_lshlrev_b32_e32 v214, 2, v22
	v_xor_b32_e32 v22, 2, v234
	v_cmp_lt_i32_e32 vcc, v22, v19
	v_lshl_add_u64 v[20:21], s[16:17], 0, v[20:21]
	s_mov_b64 s[24:25], 0x100000
	v_cndmask_b32_e32 v22, v234, v22, vcc
	v_lshlrev_b32_e32 v215, 2, v22
	v_xor_b32_e32 v22, 4, v234
	v_cmp_lt_i32_e32 vcc, v22, v19
	v_lshl_add_u64 v[208:209], v[20:21], 0, s[24:25]
	s_mov_b64 s[24:25], 0x35600000
	v_cndmask_b32_e32 v22, v234, v22, vcc
	v_lshlrev_b32_e32 v216, 2, v22
	v_xor_b32_e32 v22, 8, v234
	v_cmp_lt_i32_e32 vcc, v22, v19
	v_readlane_b32 s30, v252, 10
	v_lshl_add_u64 v[210:211], v[20:21], 0, s[24:25]
	v_cndmask_b32_e32 v22, v234, v22, vcc
	v_lshlrev_b32_e32 v217, 2, v22
	v_xor_b32_e32 v22, 16, v234
	v_cmp_lt_i32_e32 vcc, v22, v19
	v_readlane_b32 s31, v252, 11
	s_add_u32 s24, s16, s30
	v_cndmask_b32_e32 v22, v234, v22, vcc
	s_addc_u32 s25, s17, s31
	v_readlane_b32 s26, v254, 23
	v_lshlrev_b32_e32 v218, 2, v22
	v_xor_b32_e32 v22, 32, v234
	s_add_u32 s26, s16, s26
	v_readlane_b32 s27, v254, 24
	v_cmp_lt_i32_e32 vcc, v22, v19
	s_addc_u32 s27, s17, s27
	v_readlane_b32 s34, v254, 25
	v_cndmask_b32_e32 v19, v234, v22, vcc
	v_readlane_b32 s35, v254, 26
	s_add_u32 s28, s28, s34
	v_lshlrev_b32_e32 v219, 2, v19
	s_addc_u32 s29, s29, s35
	v_mov_b32_e32 v19, v1
	v_lshl_add_u64 v[212:213], s[28:29], 0, v[18:19]
	s_add_u32 s28, s4, s30
	s_addc_u32 s29, s5, s31
	v_readlane_b32 s4, v254, 38
	v_readlane_b32 s5, v254, 39
	s_add_u32 s30, s16, s4
	s_mov_b64 s[20:21], 0
	s_addc_u32 s31, s17, s5
	s_mov_b32 s36, s50
	s_andn2_b64 vcc, exec, s[22:23]
	s_cbranch_vccnz .Lycp_skip0
	v_lshl_add_u64 v[194:195], s[28:29], 0, v[0:1]
	global_load_dwordx2 v[232:233], v[194:195], off
	global_load_dwordx2 v[238:239], v[194:195], off offset:512
	global_load_dwordx2 v[242:243], v[194:195], off offset:1024
	global_load_dwordx2 v[244:245], v[194:195], off offset:1536
	v_add_co_u32_e32 v194, vcc, 0x4000000, v194
	s_nop 1
	v_addc_co_u32_e32 v195, vcc, 0, v195, vcc
	global_load_dwordx2 v[246:247], v[194:195], off
	global_load_dwordx2 v[248:249], v[194:195], off offset:512
	global_load_dwordx2 v[250:251], v[194:195], off offset:1024
	global_load_dword v241, v[194:195], off offset:1536
	global_load_dword v237, v[194:195], off offset:1540
.Lycp_skip0:
	s_mov_b64 vcc, exec
	s_mov_b64 exec, s[14:15]
	global_load_dword v240, v[206:207], off
	s_mov_b64 exec, vcc
	s_waitcnt vmcnt(0)
	s_branch .LBB0_60

.LBB0_68:
	v_cndmask_b32_e64 v178, 0, 1, s[22:23]
	v_cmp_ne_u32_e64 s[16:17], 1, v178
	s_andn2_b64 vcc, exec, s[22:23]
	s_cbranch_vccnz .LBB0_70
	v_lshl_add_u64 v[178:179], s[28:29], 0, v[0:1]
	v_mov_b32_e32 v180, v232
	v_mov_b32_e32 v181, v233
	v_mov_b32_e32 v182, v238
	v_mov_b32_e32 v183, v239
	v_mov_b32_e32 v184, v242
	v_mov_b32_e32 v185, v243
	v_mov_b32_e32 v188, v244
	v_mov_b32_e32 v189, v245
	v_mov_b32_e32 v190, v248
	v_mov_b32_e32 v191, v249
	v_mov_b32_e32 v192, v250
	v_mov_b32_e32 v193, v251
	v_mov_b32_e32 v186, v241
	v_mov_b32_e32 v187, v237
	v_lshl_add_u64 v[194:195], v[178:179], 0, s[78:79]
	v_mov_b32_e32 v178, v246
	v_mov_b32_e32 v179, v247
	s_and_b64 vcc, exec, s[34:35]
	s_cbranch_vccnz .Lycp_skip1
	global_load_dwordx2 v[232:233], v[194:195], off
	global_load_dwordx2 v[238:239], v[194:195], off offset:512
	global_load_dwordx2 v[242:243], v[194:195], off offset:1024
	global_load_dwordx2 v[244:245], v[194:195], off offset:1536
	v_add_co_u32_e32 v194, vcc, 0x4000000, v194
	s_nop 1
	v_addc_co_u32_e32 v195, vcc, 0, v195, vcc
	global_load_dwordx2 v[246:247], v[194:195], off
	global_load_dwordx2 v[248:249], v[194:195], off offset:512
	global_load_dwordx2 v[250:251], v[194:195], off offset:1024
	global_load_dword v241, v[194:195], off offset:1536
	global_load_dword v237, v[194:195], off offset:1540
	s_nop 1
.Lycp_skip1:

	v_lshlrev_b32_e32 v194, 16, v180
	v_and_b32_e32 v195, 0xffff0000, v180
	v_lshlrev_b32_e32 v180, 16, v181
	v_and_b32_e32 v181, 0xffff0000, v181

	v_lshlrev_b32_e32 v196, 16, v182
	v_and_b32_e32 v197, 0xffff0000, v182
	v_lshlrev_b32_e32 v182, 16, v183
	v_and_b32_e32 v183, 0xffff0000, v183

	v_lshlrev_b32_e32 v220, 16, v184
	v_and_b32_e32 v221, 0xffff0000, v184
	v_lshlrev_b32_e32 v184, 16, v185
	v_and_b32_e32 v185, 0xffff0000, v185

	v_lshlrev_b32_e32 v222, 16, v188
	v_and_b32_e32 v223, 0xffff0000, v188
	v_lshlrev_b32_e32 v188, 16, v189
	v_and_b32_e32 v189, 0xffff0000, v189

	v_lshlrev_b32_e32 v224, 16, v178
	v_and_b32_e32 v225, 0xffff0000, v178
	v_lshlrev_b32_e32 v178, 16, v179
	v_and_b32_e32 v179, 0xffff0000, v179

	v_lshlrev_b32_e32 v226, 16, v190
	v_and_b32_e32 v227, 0xffff0000, v190
	v_lshlrev_b32_e32 v190, 16, v191
	v_and_b32_e32 v191, 0xffff0000, v191

	v_lshlrev_b32_e32 v228, 16, v192
	v_and_b32_e32 v229, 0xffff0000, v192
	v_lshlrev_b32_e32 v192, 16, v193
	v_and_b32_e32 v193, 0xffff0000, v193

	v_lshlrev_b32_e32 v230, 16, v186
	v_and_b32_e32 v231, 0xffff0000, v186
	v_lshlrev_b32_e32 v186, 16, v187
	v_and_b32_e32 v187, 0xffff0000, v187
	v_pk_add_f32 v[186:187], v[188:189], v[186:187]
	v_pk_add_f32 v[188:189], v[194:195], v[224:225]
	v_pk_add_f32 v[194:195], v[196:197], v[226:227]
	v_pk_add_f32 v[196:197], v[220:221], v[228:229]
	v_pk_add_f32 v[220:221], v[222:223], v[230:231]
	v_pk_add_f32 v[178:179], v[180:181], v[178:179]
	v_pk_add_f32 v[180:181], v[182:183], v[190:191]
	v_pk_add_f32 v[182:183], v[184:185], v[192:193]
	v_pk_add_f32 v[24:25], v[24:25], v[180:181]
	v_pk_add_f32 v[28:29], v[28:29], v[182:183]
	s_waitcnt lgkmcnt(0)
	v_pk_add_f32 v[20:21], v[20:21], v[178:179]
	v_pk_add_f32 v[30:31], v[30:31], v[220:221]
	v_pk_add_f32 v[26:27], v[26:27], v[196:197]
	v_pk_add_f32 v[22:23], v[22:23], v[194:195]
	v_pk_add_f32 v[18:19], v[18:19], v[188:189]
	v_pk_add_f32 v[32:33], v[32:33], v[186:187]

.LBB0_80:
	v_mov_b32_e32 v237, 0x43e00000
	v_mov_b32_e32 v238, 0x42800000
	v_mov_b32_e32 v239, 0xf149f2ca
	s_mov_b32 s4, s58
	s_mov_b64 s[40:41], s[54:55]
	s_waitcnt vmcnt(0)
	s_waitcnt lgkmcnt(0)
	s_barrier
	s_mov_b64 s[6:7], exec
	v_readlane_b32 s8, v252, 2
	v_readlane_b32 s9, v252, 3
	s_and_b64 s[8:9], s[6:7], s[8:9]
	s_xor_b64 s[38:39], s[8:9], s[6:7]
	s_mov_b64 exec, s[8:9]
	s_cbranch_execz .LBB0_126
	v_readlane_b32 s5, v254, 58
	s_waitcnt vmcnt(0) expcnt(0) lgkmcnt(0)
	s_nop 0
	v_mov_b32_e32 v0, s5
	ds_read_b32 v2, v0
	v_readlane_b32 s5, v254, 59
	s_waitcnt lgkmcnt(0)
	v_cmp_ne_u32_e32 vcc, 0, v2
	v_mov_b32_e32 v0, s5
	ds_read_b32 v0, v0
	s_cbranch_vccnz .LBB0_96
	v_readlane_b32 s6, v252, 0
	v_readlane_b32 s7, v252, 1
	s_load_dwordx2 s[10:11], s[6:7], 0x4
	s_add_u32 s6, s40, 0x1000
	s_addc_u32 s7, s41, 0
	s_add_u32 s8, s40, 0x1100
	s_addc_u32 s9, s41, 0
	s_waitcnt lgkmcnt(0)
	s_mul_i32 s5, s10, s46
	s_add_u32 s10, s40, 0x1200
	s_mul_i32 s5, s5, s11
	s_addc_u32 s11, s41, 0
	s_add_u32 s12, s40, 0x1300
	s_addc_u32 s13, s41, 0
	s_mov_b32 s33, 1
	s_mov_b64 s[14:15], 0
	s_branch .LBB0_85
